# v36
# baseline (speedup 1.0000x reference)
.LBB0_9:
	s_setprio 3
	s_add_i32 s26, s35, 8
	s_cmpk_lt_i32 s26, 0x80
	s_cbranch_scc0 .Lp1_last_top
	s_lshl_b32 s24, s26, 14
	s_add_i32 s24, s24, s33
	s_waitcnt vmcnt(8)
	v_cvt_pk_bf16_f32 v2, v34, v35
	v_cvt_pk_bf16_f32 v3, v36, v37
	v_cvt_pk_bf16_f32 v10, v50, v51
	v_cvt_pk_bf16_f32 v11, v52, v53
	v_cvt_pk_bf16_f32 v4, v38, v39
	v_cvt_pk_bf16_f32 v5, v40, v41
	ds_write2_b64 v212, v[2:3], v[10:11] offset1:68
	v_cvt_pk_bf16_f32 v2, v54, v55
	v_cvt_pk_bf16_f32 v3, v56, v57
	v_cvt_pk_bf16_f32 v6, v42, v43
	v_cvt_pk_bf16_f32 v7, v44, v45
	ds_write2_b64 v215, v[4:5], v[2:3] offset0:16 offset1:84
	v_cvt_pk_bf16_f32 v2, v58, v59
	v_cvt_pk_bf16_f32 v3, v60, v61
	v_cvt_pk_bf16_f32 v8, v46, v47
	v_cvt_pk_bf16_f32 v9, v48, v49
	ds_write2_b64 v216, v[6:7], v[2:3] offset0:32 offset1:100
	v_cvt_pk_bf16_f32 v2, v62, v63
	v_cvt_pk_bf16_f32 v3, v64, v65
	ds_write2_b64 v217, v[8:9], v[2:3] offset0:48 offset1:116
	s_or_b32 s25, s24, 0x1000
	buffer_load_dwordx4 v[34:37], v204, s[12:15], s24 offen sc0 nt sc1
	buffer_load_dwordx4 v[38:41], v204, s[12:15], s25 offen sc0 nt sc1
	s_or_b32 s25, s24, 0x2000
	s_or_b32 s27, s24, 0x3000
	buffer_load_dwordx4 v[42:45], v204, s[12:15], s25 offen sc0 nt sc1
	buffer_load_dwordx4 v[46:49], v204, s[12:15], s27 offen sc0 nt sc1
	s_or_b32 s25, s24, 0x400
	s_or_b32 s27, s24, 0x1400
	buffer_load_dwordx4 v[50:53], v204, s[12:15], s25 offen sc0 nt sc1
	buffer_load_dwordx4 v[54:57], v204, s[12:15], s27 offen sc0 nt sc1
	s_or_b32 s25, s24, 0x2400
	s_or_b32 s27, s24, 0x3400
	buffer_load_dwordx4 v[58:61], v204, s[12:15], s25 offen sc0 nt sc1
	buffer_load_dwordx4 v[62:65], v204, s[12:15], s27 offen sc0 nt sc1
	s_waitcnt vmcnt(8)
	v_cvt_pk_bf16_f32 v2, v66, v67
	v_cvt_pk_bf16_f32 v3, v68, v69
	v_cvt_pk_bf16_f32 v10, v82, v83
	v_cvt_pk_bf16_f32 v11, v84, v85
	v_cvt_pk_bf16_f32 v4, v70, v71
	v_cvt_pk_bf16_f32 v5, v72, v73
	ds_write2_b64 v212, v[2:3], v[10:11] offset0:136 offset1:204
	v_cvt_pk_bf16_f32 v2, v86, v87
	v_cvt_pk_bf16_f32 v3, v88, v89
	v_cvt_pk_bf16_f32 v6, v74, v75
	v_cvt_pk_bf16_f32 v7, v76, v77
	ds_write2_b64 v215, v[4:5], v[2:3] offset0:152 offset1:220
	v_cvt_pk_bf16_f32 v2, v90, v91
	v_cvt_pk_bf16_f32 v3, v92, v93
	v_cvt_pk_bf16_f32 v8, v78, v79
	v_cvt_pk_bf16_f32 v9, v80, v81
	ds_write2_b64 v216, v[6:7], v[2:3] offset0:168 offset1:236
	v_cvt_pk_bf16_f32 v2, v94, v95
	v_cvt_pk_bf16_f32 v3, v96, v97
	ds_write2_b64 v217, v[8:9], v[2:3] offset0:184 offset1:252
	s_or_b32 s25, s24, 0x800
	s_or_b32 s27, s24, 0x1800
	buffer_load_dwordx4 v[66:69], v204, s[12:15], s25 offen sc0 nt sc1
	buffer_load_dwordx4 v[70:73], v204, s[12:15], s27 offen sc0 nt sc1
	s_or_b32 s25, s24, 0x2800
	s_or_b32 s27, s24, 0x3800
	buffer_load_dwordx4 v[74:77], v204, s[12:15], s25 offen sc0 nt sc1
	buffer_load_dwordx4 v[78:81], v204, s[12:15], s27 offen sc0 nt sc1
	s_or_b32 s25, s24, 0xc00
	s_or_b32 s27, s24, 0x1c00
	buffer_load_dwordx4 v[82:85], v204, s[12:15], s25 offen sc0 nt sc1
	buffer_load_dwordx4 v[86:89], v204, s[12:15], s27 offen sc0 nt sc1
	s_or_b32 s25, s24, 0x2c00
	s_or_b32 s24, s24, 0x3c00
	buffer_load_dwordx4 v[90:93], v204, s[12:15], s25 offen sc0 nt sc1
	buffer_load_dwordx4 v[94:97], v204, s[12:15], s24 offen sc0 nt sc1
	s_branch .LBB0_17
